# layers 1-3 gather: both nodes of a 16-lane group as one continuous edge stream (no mid-stream pipeline drain), accumulator chosen per slot by exec mask
# baseline (speedup 1.0000x reference)
.LBB5_24:
	v_or_b32_e32 v47, 1, v35
	v_add_u32_e32 v46, s24, v47
	s_mov_b32 s2, 0x186a0
	v_cmp_gt_i32_e32 vcc, s2, v46
	s_mov_b64 s[0:1], vcc
	v_min_i32_e32 v46, 0x1869f, v46
	v_lshl_add_u32 v46, v46, 8, v26
	global_load_dwordx4 v[30:33], v46, s[4:5]
	v_mov_b32_e32 v46, 0x3204
	v_lshl_add_u32 v46, v47, 2, v46
	ds_read_b32 v49, v46
	s_mov_b64 s[22:23], exec
	s_movk_i32 s3, 0x2200
	v_sub_u32_e32 v27, v44, v28
	v_lshl_add_u32 v27, v27, 2, s3
	v_lshl_add_u32 v29, v44, 8, v26
	v_mov_b32_e32 v28, v45
	v_mov_b32_e32 v48, v34
	s_waitcnt lgkmcnt(0)
	v_mov_b32_e32 v45, v49
	v_cmp_lt_i32_e64 s[2:3], v44, v45
	v_add_u32_e32 v46, 1, v44
	v_cmp_lt_i32_e64 s[16:17], v46, v45
	v_add_u32_e32 v46, 2, v44
	v_cmp_lt_i32_e64 s[18:19], v46, v45
	v_add_u32_e32 v46, 3, v44
	v_cmp_lt_i32_e64 s[20:21], v46, v45
	s_mov_b64 exec, s[2:3]
	ds_read_b32 v2, v27 offset:0
	global_load_dwordx4 v[4:7], v29, s[12:13] offset:0
	s_waitcnt lgkmcnt(0)
	v_lshl_add_u32 v2, v2, 8, v26
	global_load_dwordx4 v[8:11], v2, s[4:5]
	ds_read_b32 v2, v27 offset:16
	s_mov_b64 exec, s[16:17]
	ds_read_b32 v3, v27 offset:4
	global_load_dwordx4 v[12:15], v29, s[12:13] offset:256
	s_waitcnt lgkmcnt(0)
	v_lshl_add_u32 v3, v3, 8, v26
	global_load_dwordx4 v[16:19], v3, s[4:5]
	ds_read_b32 v3, v27 offset:20
	s_mov_b64 exec, s[18:19]
	ds_read_b32 v24, v27 offset:8
	global_load_dwordx4 v[20:23], v29, s[12:13] offset:512
	s_waitcnt lgkmcnt(0)
	v_lshl_add_u32 v24, v24, 8, v26
	global_load_dwordx4 v[50:53], v24, s[4:5]
	ds_read_b32 v24, v27 offset:24
	s_mov_b64 exec, s[20:21]
	ds_read_b32 v25, v27 offset:12
	global_load_dwordx4 v[54:57], v29, s[12:13] offset:768
	s_waitcnt lgkmcnt(0)
	v_lshl_add_u32 v25, v25, 8, v26
	global_load_dwordx4 v[58:61], v25, s[4:5]
	ds_read_b32 v25, v27 offset:28
	s_mov_b64 exec, s[22:23]
	s_waitcnt vmcnt(8)
	v_cvt_f32_f16_e32 v62, v33
	v_cvt_f32_f16_sdwa v63, v33 dst_sel:DWORD dst_unused:UNUSED_PAD src0_sel:WORD_1
	v_cvt_f32_f16_sdwa v35, v32 dst_sel:DWORD dst_unused:UNUSED_PAD src0_sel:WORD_1
	v_cvt_f32_f16_e32 v34, v32
	v_cvt_f32_f16_sdwa v33, v31 dst_sel:DWORD dst_unused:UNUSED_PAD src0_sel:WORD_1
	v_cvt_f32_f16_e32 v32, v31
	v_cvt_f32_f16_sdwa v31, v30 dst_sel:DWORD dst_unused:UNUSED_PAD src0_sel:WORD_1
	v_cvt_f32_f16_e32 v30, v30
	s_mov_b64 vcc, s[0:1]
	v_mul_f32_e32 v30, v48, v30
	v_mul_f32_e32 v31, v48, v31
	v_mul_f32_e32 v32, v48, v32
	v_mul_f32_e32 v33, v48, v33
	v_mul_f32_e32 v34, v48, v34
	v_mul_f32_e32 v35, v48, v35
	v_mul_f32_e32 v62, v48, v62
	v_mul_f32_e32 v63, v48, v63
	v_cndmask_b32_e32 v30, 0, v30, vcc
	v_cndmask_b32_e32 v31, 0, v31, vcc
	v_cndmask_b32_e32 v32, 0, v32, vcc
	v_cndmask_b32_e32 v33, 0, v33, vcc
	v_cndmask_b32_e32 v34, 0, v34, vcc
	v_cndmask_b32_e32 v35, 0, v35, vcc
	v_cndmask_b32_e32 v62, 0, v62, vcc
	v_cndmask_b32_e32 v63, 0, v63, vcc
	s_cmp_eq_u64 s[2:3], 0
	s_cbranch_scc1 .Ll1m_done
.Ll1m_loop:
	s_mov_b64 exec, s[2:3]
	s_waitcnt vmcnt(6)
	v_fma_mix_f32 v46, v8, 1.0, v4 op_sel_hi:[1,0,1]
	v_fma_mix_f32 v4, v8, 1.0, v4 op_sel:[1,0,1] op_sel_hi:[1,0,1]
	v_max_f32_e32 v8, 0, v46
	v_max_f32_e32 v4, 0, v4
	v_fma_mix_f32 v46, v9, 1.0, v5 op_sel_hi:[1,0,1]
	v_fma_mix_f32 v5, v9, 1.0, v5 op_sel:[1,0,1] op_sel_hi:[1,0,1]
	v_max_f32_e32 v9, 0, v46
	v_max_f32_e32 v5, 0, v5
	v_fma_mix_f32 v46, v10, 1.0, v6 op_sel_hi:[1,0,1]
	v_fma_mix_f32 v6, v10, 1.0, v6 op_sel:[1,0,1] op_sel_hi:[1,0,1]
	v_max_f32_e32 v10, 0, v46
	v_max_f32_e32 v6, 0, v6
	v_fma_mix_f32 v46, v11, 1.0, v7 op_sel_hi:[1,0,1]
	v_fma_mix_f32 v7, v11, 1.0, v7 op_sel:[1,0,1] op_sel_hi:[1,0,1]
	v_max_f32_e32 v11, 0, v46
	v_max_f32_e32 v7, 0, v7
	v_cmp_lt_i32_e64 s[0:1], v44, v28
	s_xor_b64 s[14:15], s[0:1], s[2:3]
	s_mov_b64 exec, s[0:1]
	v_add_f32_e32 v42, v42, v8
	v_add_f32_e32 v43, v43, v4
	v_add_f32_e32 v40, v40, v9
	v_add_f32_e32 v41, v41, v5
	v_add_f32_e32 v38, v38, v10
	v_add_f32_e32 v39, v39, v6
	v_add_f32_e32 v36, v36, v11
	v_add_f32_e32 v37, v37, v7
	s_mov_b64 exec, s[14:15]
	v_add_f32_e32 v30, v30, v8
	v_add_f32_e32 v31, v31, v4
	v_add_f32_e32 v32, v32, v9
	v_add_f32_e32 v33, v33, v5
	v_add_f32_e32 v34, v34, v10
	v_add_f32_e32 v35, v35, v6
	v_add_f32_e32 v62, v62, v11
	v_add_f32_e32 v63, v63, v7
	s_mov_b64 exec, s[2:3]
	v_add_u32_e32 v48, 4, v44
	v_cmp_lt_i32_e64 s[2:3], v48, v45
	s_mov_b64 exec, s[2:3]
	global_load_dwordx4 v[4:7], v29, s[12:13] offset:1024
	s_waitcnt lgkmcnt(0)
	v_lshl_add_u32 v2, v2, 8, v26
	global_load_dwordx4 v[8:11], v2, s[4:5]
	ds_read_b32 v2, v27 offset:32
	s_mov_b64 exec, s[16:17]
	s_waitcnt vmcnt(6)
	v_fma_mix_f32 v46, v16, 1.0, v12 op_sel_hi:[1,0,1]
	v_fma_mix_f32 v12, v16, 1.0, v12 op_sel:[1,0,1] op_sel_hi:[1,0,1]
	v_max_f32_e32 v16, 0, v46
	v_max_f32_e32 v12, 0, v12
	v_fma_mix_f32 v46, v17, 1.0, v13 op_sel_hi:[1,0,1]
	v_fma_mix_f32 v13, v17, 1.0, v13 op_sel:[1,0,1] op_sel_hi:[1,0,1]
	v_max_f32_e32 v17, 0, v46
	v_max_f32_e32 v13, 0, v13
	v_fma_mix_f32 v46, v18, 1.0, v14 op_sel_hi:[1,0,1]
	v_fma_mix_f32 v14, v18, 1.0, v14 op_sel:[1,0,1] op_sel_hi:[1,0,1]
	v_max_f32_e32 v18, 0, v46
	v_max_f32_e32 v14, 0, v14
	v_fma_mix_f32 v46, v19, 1.0, v15 op_sel_hi:[1,0,1]
	v_fma_mix_f32 v15, v19, 1.0, v15 op_sel:[1,0,1] op_sel_hi:[1,0,1]
	v_max_f32_e32 v19, 0, v46
	v_max_f32_e32 v15, 0, v15
	v_add_u32_e32 v48, 1, v44
	v_cmp_lt_i32_e64 s[0:1], v48, v28
	s_xor_b64 s[14:15], s[0:1], s[16:17]
	s_mov_b64 exec, s[0:1]
	v_add_f32_e32 v42, v42, v16
	v_add_f32_e32 v43, v43, v12
	v_add_f32_e32 v40, v40, v17
	v_add_f32_e32 v41, v41, v13
	v_add_f32_e32 v38, v38, v18
	v_add_f32_e32 v39, v39, v14
	v_add_f32_e32 v36, v36, v19
	v_add_f32_e32 v37, v37, v15
	s_mov_b64 exec, s[14:15]
	v_add_f32_e32 v30, v30, v16
	v_add_f32_e32 v31, v31, v12
	v_add_f32_e32 v32, v32, v17
	v_add_f32_e32 v33, v33, v13
	v_add_f32_e32 v34, v34, v18
	v_add_f32_e32 v35, v35, v14
	v_add_f32_e32 v62, v62, v19
	v_add_f32_e32 v63, v63, v15
	s_mov_b64 exec, s[16:17]
	v_add_u32_e32 v48, 5, v44
	v_cmp_lt_i32_e64 s[16:17], v48, v45
	s_mov_b64 exec, s[16:17]
	global_load_dwordx4 v[12:15], v29, s[12:13] offset:1280
	s_waitcnt lgkmcnt(0)
	v_lshl_add_u32 v3, v3, 8, v26
	global_load_dwordx4 v[16:19], v3, s[4:5]
	ds_read_b32 v3, v27 offset:36
	s_mov_b64 exec, s[18:19]
	s_waitcnt vmcnt(6)
	v_fma_mix_f32 v46, v50, 1.0, v20 op_sel_hi:[1,0,1]
	v_fma_mix_f32 v20, v50, 1.0, v20 op_sel:[1,0,1] op_sel_hi:[1,0,1]
	v_max_f32_e32 v50, 0, v46
	v_max_f32_e32 v20, 0, v20
	v_fma_mix_f32 v46, v51, 1.0, v21 op_sel_hi:[1,0,1]
	v_fma_mix_f32 v21, v51, 1.0, v21 op_sel:[1,0,1] op_sel_hi:[1,0,1]
	v_max_f32_e32 v51, 0, v46
	v_max_f32_e32 v21, 0, v21
	v_fma_mix_f32 v46, v52, 1.0, v22 op_sel_hi:[1,0,1]
	v_fma_mix_f32 v22, v52, 1.0, v22 op_sel:[1,0,1] op_sel_hi:[1,0,1]
	v_max_f32_e32 v52, 0, v46
	v_max_f32_e32 v22, 0, v22
	v_fma_mix_f32 v46, v53, 1.0, v23 op_sel_hi:[1,0,1]
	v_fma_mix_f32 v23, v53, 1.0, v23 op_sel:[1,0,1] op_sel_hi:[1,0,1]
	v_max_f32_e32 v53, 0, v46
	v_max_f32_e32 v23, 0, v23
	v_add_u32_e32 v48, 2, v44
	v_cmp_lt_i32_e64 s[0:1], v48, v28
	s_xor_b64 s[14:15], s[0:1], s[18:19]
	s_mov_b64 exec, s[0:1]
	v_add_f32_e32 v42, v42, v50
	v_add_f32_e32 v43, v43, v20
	v_add_f32_e32 v40, v40, v51
	v_add_f32_e32 v41, v41, v21
	v_add_f32_e32 v38, v38, v52
	v_add_f32_e32 v39, v39, v22
	v_add_f32_e32 v36, v36, v53
	v_add_f32_e32 v37, v37, v23
	s_mov_b64 exec, s[14:15]
	v_add_f32_e32 v30, v30, v50
	v_add_f32_e32 v31, v31, v20
	v_add_f32_e32 v32, v32, v51
	v_add_f32_e32 v33, v33, v21
	v_add_f32_e32 v34, v34, v52
	v_add_f32_e32 v35, v35, v22
	v_add_f32_e32 v62, v62, v53
	v_add_f32_e32 v63, v63, v23
	s_mov_b64 exec, s[18:19]
	v_add_u32_e32 v48, 6, v44
	v_cmp_lt_i32_e64 s[18:19], v48, v45
	s_mov_b64 exec, s[18:19]
	global_load_dwordx4 v[20:23], v29, s[12:13] offset:1536
	s_waitcnt lgkmcnt(0)
	v_lshl_add_u32 v24, v24, 8, v26
	global_load_dwordx4 v[50:53], v24, s[4:5]
	ds_read_b32 v24, v27 offset:40
	s_mov_b64 exec, s[20:21]
	s_waitcnt vmcnt(6)
	v_fma_mix_f32 v46, v58, 1.0, v54 op_sel_hi:[1,0,1]
	v_fma_mix_f32 v54, v58, 1.0, v54 op_sel:[1,0,1] op_sel_hi:[1,0,1]
	v_max_f32_e32 v58, 0, v46
	v_max_f32_e32 v54, 0, v54
	v_fma_mix_f32 v46, v59, 1.0, v55 op_sel_hi:[1,0,1]
	v_fma_mix_f32 v55, v59, 1.0, v55 op_sel:[1,0,1] op_sel_hi:[1,0,1]
	v_max_f32_e32 v59, 0, v46
	v_max_f32_e32 v55, 0, v55
	v_fma_mix_f32 v46, v60, 1.0, v56 op_sel_hi:[1,0,1]
	v_fma_mix_f32 v56, v60, 1.0, v56 op_sel:[1,0,1] op_sel_hi:[1,0,1]
	v_max_f32_e32 v60, 0, v46
	v_max_f32_e32 v56, 0, v56
	v_fma_mix_f32 v46, v61, 1.0, v57 op_sel_hi:[1,0,1]
	v_fma_mix_f32 v57, v61, 1.0, v57 op_sel:[1,0,1] op_sel_hi:[1,0,1]
	v_max_f32_e32 v61, 0, v46
	v_max_f32_e32 v57, 0, v57
	v_add_u32_e32 v48, 3, v44
	v_cmp_lt_i32_e64 s[0:1], v48, v28
	s_xor_b64 s[14:15], s[0:1], s[20:21]
	s_mov_b64 exec, s[0:1]
	v_add_f32_e32 v42, v42, v58
	v_add_f32_e32 v43, v43, v54
	v_add_f32_e32 v40, v40, v59
	v_add_f32_e32 v41, v41, v55
	v_add_f32_e32 v38, v38, v60
	v_add_f32_e32 v39, v39, v56
	v_add_f32_e32 v36, v36, v61
	v_add_f32_e32 v37, v37, v57
	s_mov_b64 exec, s[14:15]
	v_add_f32_e32 v30, v30, v58
	v_add_f32_e32 v31, v31, v54
	v_add_f32_e32 v32, v32, v59
	v_add_f32_e32 v33, v33, v55
	v_add_f32_e32 v34, v34, v60
	v_add_f32_e32 v35, v35, v56
	v_add_f32_e32 v62, v62, v61
	v_add_f32_e32 v63, v63, v57
	s_mov_b64 exec, s[20:21]
	v_add_u32_e32 v48, 7, v44
	v_cmp_lt_i32_e64 s[20:21], v48, v45
	s_mov_b64 exec, s[20:21]
	global_load_dwordx4 v[54:57], v29, s[12:13] offset:1792
	s_waitcnt lgkmcnt(0)
	v_lshl_add_u32 v25, v25, 8, v26
	global_load_dwordx4 v[58:61], v25, s[4:5]
	ds_read_b32 v25, v27 offset:44
	s_mov_b64 exec, s[22:23]
	v_add_u32_e32 v44, 4, v44
	v_add_u32_e32 v27, 16, v27
	v_add_u32_e32 v29, 0x400, v29
	s_cmp_lg_u64 s[2:3], 0
	s_cbranch_scc1 .Ll1m_loop
.Ll1m_done:
	s_movk_i32 s2, 0x110
	v_cvt_pk_f16_f32 v5, v36, v37
	v_cvt_pk_f16_f32 v4, v38, v39
	v_cvt_pk_f16_f32 v3, v40, v41
	v_cvt_pk_f16_f32 v2, v42, v43
	v_lshrrev_b32_e32 v27, 3, v0
	v_and_b32_e32 v46, 30, v27
	v_mad_u32_u24 v46, v46, s2, v26
	ds_write_b128 v46, v[2:5]
	v_or_b32_e32 v27, 1, v27
	v_mov_b32_e32 v50, v62
	v_mov_b32_e32 v51, v63
	v_mov_b32_e32 v48, v34
	v_mov_b32_e32 v49, v35
	v_mov_b32_e32 v46, v32
	v_mov_b32_e32 v47, v33
	v_mov_b32_e32 v34, v30
	v_mov_b32_e32 v35, v31
	s_branch .LBB5_61
